# P5: new unit's gathered A offsets copied from the values already computed in the last K trip (kept alive by the hand-written epilogue) instead of recomputing them after the epilogue
# baseline (speedup 1.0000x reference)
; #define PG8_LAS __attribute__((address_space(3)))
;     __device__ __forceinline__ unsigned raw_off(const Unit& u, int h, int R, unsigned raw) const { const int pos = u.rb * 256 + h * 128 + R; return (pos < u.cnt ? (raw >> 2) : 0u) * rowbytes; }
; template <class Epi, class Sched, bool GATHER, int MODE>
; __device__ __forceinline__ void gemm_phase(PG8_LAS unsigned char* lds, PG8_LAS unsigned* scr, const Gemm g, const Sched& S, const Epi& E, int tid_in) {
;     ...
;     auto gather_read = [&](const Unit& uu) { u32x4 o; int tz = tid; asm volatile("" : "+v"(tz));
; #pragma unroll
;         for (int i = 0; i < 2; ++i) { int R, C; stage_rc(tz * 16 + i * 8192, R, C);
; #pragma unroll
;             for (int h = 0; h < 2; ++h) o[2 * h + i] = S.raw_off(uu, h, R, *((const PG8_LAS unsigned*)(scr + 1024) + (2 * h + i) * 512 + tz)) + (unsigned)C * 2u; }
;         return o; };
;     ...
;         cur = nxt; cA = nA; cB = nB; ++ui;
;         if (GATHER) { const u32x4 nx = gather_read(cur); c0[0] = nx[0]; c0[1] = nx[1]; c1[0] = nx[2]; c1[1] = nx[3]; }
.LBB0_785:
	v_mov_b32_e32 v185, v40
	v_mov_b32_e32 v202, v41
	v_mov_b32_e32 v201, v42
	v_mov_b32_e32 v203, v43
	s_mov_b64 s[10:11], 0

;     __device__ __forceinline__ void operator()(const i32x4 (&acc)[2][2][4][2], const Unit& u, int wr, int wc, int fr, int fq, PG8_LAS unsigned* scr) const {
;     ...
;         for (int ai = 0; ai < 2; ++ai)
; #pragma unroll
;             for (int mp = 0; mp < 4; mp += 2) { unsigned wp[2][2];
; #pragma unroll
;                 for (int hm = 0; hm < 2; ++hm) { const int m = mp + hm; const int r = ai * HALF + wr * 64 + m * 16 + fr; const float rs = __uint_as_float(scr[r]); float o[8];
; #pragma unroll
;                     for (int n = 0; n < 2; ++n) { const f32x4 sgr = csg[n] * rs, sur = csu[n] * rs;
; #pragma unroll
;                         for (int q = 0; q < 4; ++q) { const float h = fminf(__builtin_fmaf((float)acc[ai][0][m][n][q], sgr[q], bgv[n][q]), 7.0f * C2), up = fminf(fmaxf(__builtin_fmaf((float)acc[ai][1][m][n][q], sur[q], buv[n][q]), -7.0f), 7.0f);
;                             const float sg = __builtin_amdgcn_rcpf(1.0f + __builtin_amdgcn_exp2f(-h)); o[4 * n + q] = __builtin_fmaf(up, ACT_SC / C2, ACT_SC / C2) * (h * sg); } }
;                     int w0 = __builtin_amdgcn_cvt_pk_fp8_f32(o[0], o[1], 0, false); w0 = __builtin_amdgcn_cvt_pk_fp8_f32(o[2], o[3], w0, true);
;                     int w1 = __builtin_amdgcn_cvt_pk_fp8_f32(o[4], o[5], 0, false); w1 = __builtin_amdgcn_cvt_pk_fp8_f32(o[6], o[7], w1, true);
;                     wp[hm][0] = (unsigned)w0; wp[hm][1] = (unsigned)w1; }
.Lp5_epi_nobar:
	v_cvt_f32_i32_e32 v96, v96
	v_cvt_f32_i32_e32 v97, v97
	v_cvt_f32_i32_e32 v98, v98
	v_cvt_f32_i32_e32 v99, v99
	v_cvt_f32_i32_e32 v100, v100
	v_cvt_f32_i32_e32 v101, v101
	v_cvt_f32_i32_e32 v102, v102
	v_cvt_f32_i32_e32 v103, v103
	v_pk_mul_f32 v[160:161], v[144:145], v[154:155] op_sel_hi:[1,0]
	v_pk_mul_f32 v[162:163], v[146:147], v[154:155] op_sel_hi:[1,0]
	v_pk_fma_f32 v[96:97], v[96:97], v[160:161], v[136:137]
	v_pk_fma_f32 v[98:99], v[98:99], v[162:163], v[138:139]
	v_pk_mul_f32 v[160:161], v[148:149], v[154:155] op_sel_hi:[1,0]
	v_pk_mul_f32 v[162:163], v[150:151], v[154:155] op_sel_hi:[1,0]
	v_min_f32_e32 v96, 0x41898193, v96
	v_min_f32_e32 v97, 0x41898193, v97
	v_min_f32_e32 v98, 0x41898193, v98
	v_min_f32_e32 v99, 0x41898193, v99
	v_pk_fma_f32 v[100:101], v[100:101], v[160:161], v[140:141]
	v_pk_fma_f32 v[102:103], v[102:103], v[162:163], v[142:143]
	v_exp_f32_e64 v160, -v96
	v_exp_f32_e64 v161, -v97
	v_exp_f32_e64 v162, -v98
	v_exp_f32_e64 v163, -v99
	v_med3_f32 v100, v100, s8, v199
	v_med3_f32 v101, v101, s8, v199
	v_med3_f32 v102, v102, s8, v199
	v_med3_f32 v103, v103, s8, v199
	v_pk_add_f32 v[160:161], v[160:161], 1.0 op_sel_hi:[1,0]
	v_pk_add_f32 v[162:163], v[162:163], 1.0 op_sel_hi:[1,0]
	v_pk_fma_f32 v[100:101], v[100:101], s[100:101], s[100:101]
	v_pk_fma_f32 v[102:103], v[102:103], s[100:101], s[100:101]
	v_rcp_f32_e32 v160, v160
	v_rcp_f32_e32 v161, v161
	v_rcp_f32_e32 v162, v162
	v_rcp_f32_e32 v163, v163
	v_nop
	v_pk_mul_f32 v[96:97], v[96:97], v[160:161]
	v_pk_mul_f32 v[98:99], v[98:99], v[162:163]
	v_pk_mul_f32 v[96:97], v[100:101], v[96:97]
	v_pk_mul_f32 v[98:99], v[102:103], v[98:99]
	v_cvt_pk_fp8_f32 v96, v96, v97
	v_cvt_pk_fp8_f32 v96, v98, v99 op_sel:[0,0,1]
	v_cvt_f32_i32_e32 v80, v80
	v_cvt_f32_i32_e32 v81, v81
	v_cvt_f32_i32_e32 v82, v82
	v_cvt_f32_i32_e32 v83, v83
	v_cvt_f32_i32_e32 v84, v84
	v_cvt_f32_i32_e32 v85, v85
	v_cvt_f32_i32_e32 v86, v86
	v_cvt_f32_i32_e32 v87, v87
	v_pk_mul_f32 v[202:203], v[144:145], v[154:155] op_sel:[0,1] op_sel_hi:[1,1]
	v_pk_mul_f32 v[204:205], v[146:147], v[154:155] op_sel:[0,1] op_sel_hi:[1,1]
	v_pk_fma_f32 v[80:81], v[80:81], v[202:203], v[136:137]
	v_pk_fma_f32 v[82:83], v[82:83], v[204:205], v[138:139]
	v_pk_mul_f32 v[202:203], v[148:149], v[154:155] op_sel:[0,1] op_sel_hi:[1,1]
	v_pk_mul_f32 v[204:205], v[150:151], v[154:155] op_sel:[0,1] op_sel_hi:[1,1]
	v_min_f32_e32 v80, 0x41898193, v80
	v_min_f32_e32 v81, 0x41898193, v81
	v_min_f32_e32 v82, 0x41898193, v82
	v_min_f32_e32 v83, 0x41898193, v83
	v_pk_fma_f32 v[84:85], v[84:85], v[202:203], v[140:141]
	v_pk_fma_f32 v[86:87], v[86:87], v[204:205], v[142:143]
	v_exp_f32_e64 v202, -v80
	v_exp_f32_e64 v203, -v81
	v_exp_f32_e64 v204, -v82
	v_exp_f32_e64 v205, -v83
	v_med3_f32 v84, v84, s8, v199
	v_med3_f32 v85, v85, s8, v199
	v_med3_f32 v86, v86, s8, v199
	v_med3_f32 v87, v87, s8, v199
	v_pk_add_f32 v[202:203], v[202:203], 1.0 op_sel_hi:[1,0]
	v_pk_add_f32 v[204:205], v[204:205], 1.0 op_sel_hi:[1,0]
	v_pk_fma_f32 v[84:85], v[84:85], s[100:101], s[100:101]
	v_pk_fma_f32 v[86:87], v[86:87], s[100:101], s[100:101]
	v_rcp_f32_e32 v202, v202
	v_rcp_f32_e32 v203, v203
	v_rcp_f32_e32 v204, v204
	v_rcp_f32_e32 v205, v205
	v_nop
	v_pk_mul_f32 v[80:81], v[80:81], v[202:203]
	v_pk_mul_f32 v[82:83], v[82:83], v[204:205]
	v_pk_mul_f32 v[80:81], v[84:85], v[80:81]
	v_pk_mul_f32 v[82:83], v[86:87], v[82:83]
	v_cvt_pk_fp8_f32 v98, v80, v81
	v_cvt_pk_fp8_f32 v98, v82, v83 op_sel:[0,0,1]
	v_cvt_f32_i32_e32 v64, v64
	v_cvt_f32_i32_e32 v65, v65
	v_cvt_f32_i32_e32 v66, v66
	v_cvt_f32_i32_e32 v67, v67
	v_cvt_f32_i32_e32 v68, v68
	v_cvt_f32_i32_e32 v69, v69
	v_cvt_f32_i32_e32 v70, v70
	v_cvt_f32_i32_e32 v71, v71
	v_pk_mul_f32 v[160:161], v[144:145], v[156:157] op_sel_hi:[1,0]
	v_pk_mul_f32 v[162:163], v[146:147], v[156:157] op_sel_hi:[1,0]
	v_pk_fma_f32 v[64:65], v[64:65], v[160:161], v[136:137]
	v_pk_fma_f32 v[66:67], v[66:67], v[162:163], v[138:139]
	v_pk_mul_f32 v[160:161], v[148:149], v[156:157] op_sel_hi:[1,0]
	v_pk_mul_f32 v[162:163], v[150:151], v[156:157] op_sel_hi:[1,0]
	v_min_f32_e32 v64, 0x41898193, v64
	v_min_f32_e32 v65, 0x41898193, v65
	v_min_f32_e32 v66, 0x41898193, v66
	v_min_f32_e32 v67, 0x41898193, v67
	v_pk_fma_f32 v[68:69], v[68:69], v[160:161], v[140:141]
	v_pk_fma_f32 v[70:71], v[70:71], v[162:163], v[142:143]
	v_exp_f32_e64 v160, -v64
	v_exp_f32_e64 v161, -v65
	v_exp_f32_e64 v162, -v66
	v_exp_f32_e64 v163, -v67
	v_med3_f32 v68, v68, s8, v199
	v_med3_f32 v69, v69, s8, v199
	v_med3_f32 v70, v70, s8, v199
	v_med3_f32 v71, v71, s8, v199
	v_pk_add_f32 v[160:161], v[160:161], 1.0 op_sel_hi:[1,0]
	v_pk_add_f32 v[162:163], v[162:163], 1.0 op_sel_hi:[1,0]
	v_pk_fma_f32 v[68:69], v[68:69], s[100:101], s[100:101]
	v_pk_fma_f32 v[70:71], v[70:71], s[100:101], s[100:101]
	v_rcp_f32_e32 v160, v160
	v_rcp_f32_e32 v161, v161
	v_rcp_f32_e32 v162, v162
	v_rcp_f32_e32 v163, v163
	v_nop
	v_pk_mul_f32 v[64:65], v[64:65], v[160:161]
	v_pk_mul_f32 v[66:67], v[66:67], v[162:163]
	v_pk_mul_f32 v[64:65], v[68:69], v[64:65]
	v_pk_mul_f32 v[66:67], v[70:71], v[66:67]
	v_cvt_pk_fp8_f32 v64, v64, v65
	v_cvt_pk_fp8_f32 v64, v66, v67 op_sel:[0,0,1]
	v_cvt_f32_i32_e32 v44, v44
	v_cvt_f32_i32_e32 v45, v45
	v_cvt_f32_i32_e32 v46, v46
	v_cvt_f32_i32_e32 v47, v47
	v_cvt_f32_i32_e32 v48, v48
	v_cvt_f32_i32_e32 v49, v49
	v_cvt_f32_i32_e32 v50, v50
	v_cvt_f32_i32_e32 v51, v51
	v_pk_mul_f32 v[202:203], v[144:145], v[156:157] op_sel:[0,1] op_sel_hi:[1,1]
	v_pk_mul_f32 v[204:205], v[146:147], v[156:157] op_sel:[0,1] op_sel_hi:[1,1]
	v_pk_fma_f32 v[44:45], v[44:45], v[202:203], v[136:137]
	v_pk_fma_f32 v[46:47], v[46:47], v[204:205], v[138:139]
; #define PG8_LAS __attribute__((address_space(3)))
;     __device__ __forceinline__ void operator()(const i32x4 (&acc)[2][2][4][2], const Unit& u, int wr, int wc, int fr, int fq, PG8_LAS unsigned* scr) const {
;     ...
;         for (int n = 0; n < 2; ++n) { bgv[n] = *(const PG8_LAS f32x4*)(scr + 512 + cl + 4 * n) * C2; buv[n] = *(const PG8_LAS f32x4*)(scr + 512 + 128 + cl + 4 * n);
;             csg[n] = *(const PG8_LAS f32x4*)(scr + 256 + cl + 4 * n) * (C2 / 127.0f); csu[n] = *(const PG8_LAS f32x4*)(scr + 256 + 128 + cl + 4 * n) * (1.0f / 127.0f); }
;     ...
;                 for (int hm = 0; hm < 2; ++hm) { const int m = mp + hm; const int r = ai * HALF + wr * 64 + m * 16 + fr; const float rs = __uint_as_float(scr[r]); float o[8];
; #pragma unroll
;                     for (int n = 0; n < 2; ++n) { const f32x4 sgr = csg[n] * rs, sur = csu[n] * rs;
; #pragma unroll
;                         for (int q = 0; q < 4; ++q) { const float h = fminf(__builtin_fmaf((float)acc[ai][0][m][n][q], sgr[q], bgv[n][q]), 7.0f * C2), up = fminf(fmaxf(__builtin_fmaf((float)acc[ai][1][m][n][q], sur[q], buv[n][q]), -7.0f), 7.0f);
;                             const float sg = __builtin_amdgcn_rcpf(1.0f + __builtin_amdgcn_exp2f(-h)); o[4 * n + q] = __builtin_fmaf(up, ACT_SC / C2, ACT_SC / C2) * (h * sg); } }
;                     int w0 = __builtin_amdgcn_cvt_pk_fp8_f32(o[0], o[1], 0, false); w0 = __builtin_amdgcn_cvt_pk_fp8_f32(o[2], o[3], w0, true);
;                     int w1 = __builtin_amdgcn_cvt_pk_fp8_f32(o[4], o[5], 0, false); w1 = __builtin_amdgcn_cvt_pk_fp8_f32(o[6], o[7], w1, true);
;                     wp[hm][0] = (unsigned)w0; wp[hm][1] = (unsigned)w1; }
	v_pk_mul_f32 v[202:203], v[148:149], v[156:157] op_sel:[0,1] op_sel_hi:[1,1]
	v_pk_mul_f32 v[204:205], v[150:151], v[156:157] op_sel:[0,1] op_sel_hi:[1,1]
	v_min_f32_e32 v44, 0x41898193, v44
	v_min_f32_e32 v45, 0x41898193, v45
	v_min_f32_e32 v46, 0x41898193, v46
	v_min_f32_e32 v47, 0x41898193, v47
	v_pk_fma_f32 v[48:49], v[48:49], v[202:203], v[140:141]
	v_pk_fma_f32 v[50:51], v[50:51], v[204:205], v[142:143]
	v_exp_f32_e64 v202, -v44
	v_exp_f32_e64 v203, -v45
	v_exp_f32_e64 v204, -v46
	v_exp_f32_e64 v205, -v47
	v_med3_f32 v48, v48, s8, v199
	v_med3_f32 v49, v49, s8, v199
	v_med3_f32 v50, v50, s8, v199
	v_med3_f32 v51, v51, s8, v199
	v_pk_add_f32 v[202:203], v[202:203], 1.0 op_sel_hi:[1,0]
	v_pk_add_f32 v[204:205], v[204:205], 1.0 op_sel_hi:[1,0]
	v_pk_fma_f32 v[48:49], v[48:49], s[100:101], s[100:101]
	v_pk_fma_f32 v[50:51], v[50:51], s[100:101], s[100:101]
	v_rcp_f32_e32 v202, v202
	v_rcp_f32_e32 v203, v203
	v_rcp_f32_e32 v204, v204
	v_rcp_f32_e32 v205, v205
	v_nop
	v_pk_mul_f32 v[44:45], v[44:45], v[202:203]
	v_pk_mul_f32 v[46:47], v[46:47], v[204:205]
	v_pk_mul_f32 v[44:45], v[48:49], v[44:45]
	v_pk_mul_f32 v[46:47], v[50:51], v[46:47]
	v_cvt_pk_fp8_f32 v66, v44, v45
	v_cvt_pk_fp8_f32 v66, v46, v47 op_sel:[0,0,1]
	v_cvt_f32_i32_e32 v24, v24
	v_cvt_f32_i32_e32 v25, v25
	v_cvt_f32_i32_e32 v26, v26
	v_cvt_f32_i32_e32 v27, v27
	v_cvt_f32_i32_e32 v28, v28
	v_cvt_f32_i32_e32 v29, v29
	v_cvt_f32_i32_e32 v30, v30
	v_cvt_f32_i32_e32 v31, v31
	v_pk_mul_f32 v[160:161], v[144:145], v[158:159] op_sel_hi:[1,0]
	v_pk_mul_f32 v[162:163], v[146:147], v[158:159] op_sel_hi:[1,0]
	v_pk_fma_f32 v[24:25], v[24:25], v[160:161], v[136:137]
	v_pk_fma_f32 v[26:27], v[26:27], v[162:163], v[138:139]
	v_pk_mul_f32 v[160:161], v[148:149], v[158:159] op_sel_hi:[1,0]
	v_pk_mul_f32 v[162:163], v[150:151], v[158:159] op_sel_hi:[1,0]
	v_min_f32_e32 v24, 0x41898193, v24
	v_min_f32_e32 v25, 0x41898193, v25
	v_min_f32_e32 v26, 0x41898193, v26
	v_min_f32_e32 v27, 0x41898193, v27
	v_pk_fma_f32 v[28:29], v[28:29], v[160:161], v[140:141]
	v_pk_fma_f32 v[30:31], v[30:31], v[162:163], v[142:143]
	v_exp_f32_e64 v160, -v24
	v_exp_f32_e64 v161, -v25
	v_exp_f32_e64 v162, -v26
	v_exp_f32_e64 v163, -v27
	v_med3_f32 v28, v28, s8, v199
	v_med3_f32 v29, v29, s8, v199
	v_med3_f32 v30, v30, s8, v199
	v_med3_f32 v31, v31, s8, v199
	v_pk_add_f32 v[160:161], v[160:161], 1.0 op_sel_hi:[1,0]
	v_pk_add_f32 v[162:163], v[162:163], 1.0 op_sel_hi:[1,0]
	v_pk_fma_f32 v[28:29], v[28:29], s[100:101], s[100:101]
	v_pk_fma_f32 v[30:31], v[30:31], s[100:101], s[100:101]
	v_rcp_f32_e32 v160, v160
	v_rcp_f32_e32 v161, v161
	v_rcp_f32_e32 v162, v162
	v_rcp_f32_e32 v163, v163
	v_nop
	v_pk_mul_f32 v[24:25], v[24:25], v[160:161]
	v_pk_mul_f32 v[26:27], v[26:27], v[162:163]
	v_pk_mul_f32 v[24:25], v[28:29], v[24:25]
	v_pk_mul_f32 v[26:27], v[30:31], v[26:27]
	v_cvt_pk_fp8_f32 v24, v24, v25
	v_cvt_pk_fp8_f32 v24, v26, v27 op_sel:[0,0,1]
	v_cvt_f32_i32_e32 v8, v8
	v_cvt_f32_i32_e32 v9, v9
	v_cvt_f32_i32_e32 v10, v10
	v_cvt_f32_i32_e32 v11, v11
	v_cvt_f32_i32_e32 v12, v12
	v_cvt_f32_i32_e32 v13, v13
	v_cvt_f32_i32_e32 v14, v14
	v_cvt_f32_i32_e32 v15, v15
	v_pk_mul_f32 v[202:203], v[144:145], v[158:159] op_sel:[0,1] op_sel_hi:[1,1]
	v_pk_mul_f32 v[204:205], v[146:147], v[158:159] op_sel:[0,1] op_sel_hi:[1,1]
	v_pk_fma_f32 v[8:9], v[8:9], v[202:203], v[136:137]
	v_pk_fma_f32 v[10:11], v[10:11], v[204:205], v[138:139]
	v_pk_mul_f32 v[202:203], v[148:149], v[158:159] op_sel:[0,1] op_sel_hi:[1,1]
	v_pk_mul_f32 v[204:205], v[150:151], v[158:159] op_sel:[0,1] op_sel_hi:[1,1]
	v_min_f32_e32 v8, 0x41898193, v8
	v_min_f32_e32 v9, 0x41898193, v9
	v_min_f32_e32 v10, 0x41898193, v10
	v_min_f32_e32 v11, 0x41898193, v11
	v_pk_fma_f32 v[12:13], v[12:13], v[202:203], v[140:141]
	v_pk_fma_f32 v[14:15], v[14:15], v[204:205], v[142:143]
	v_exp_f32_e64 v202, -v8
	v_exp_f32_e64 v203, -v9
	v_exp_f32_e64 v204, -v10
	v_exp_f32_e64 v205, -v11
	v_med3_f32 v12, v12, s8, v199
	v_med3_f32 v13, v13, s8, v199
	v_med3_f32 v14, v14, s8, v199
	v_med3_f32 v15, v15, s8, v199
	v_pk_add_f32 v[202:203], v[202:203], 1.0 op_sel_hi:[1,0]
	v_pk_add_f32 v[204:205], v[204:205], 1.0 op_sel_hi:[1,0]
	v_pk_fma_f32 v[12:13], v[12:13], s[100:101], s[100:101]
	v_pk_fma_f32 v[14:15], v[14:15], s[100:101], s[100:101]
	v_rcp_f32_e32 v202, v202
	v_rcp_f32_e32 v203, v203
	v_rcp_f32_e32 v204, v204
	v_rcp_f32_e32 v205, v205
	v_nop
	v_pk_mul_f32 v[8:9], v[8:9], v[202:203]
	v_pk_mul_f32 v[10:11], v[10:11], v[204:205]
	v_pk_mul_f32 v[8:9], v[12:13], v[8:9]
	v_pk_mul_f32 v[10:11], v[14:15], v[10:11]
	v_cvt_pk_fp8_f32 v26, v8, v9
	v_cvt_pk_fp8_f32 v26, v10, v11 op_sel:[0,0,1]
	v_add_u32_e32 v160, 0x21110, v208
	ds_read_b128 v[136:139], v160
	v_add_u32_e32 v160, 0x21310, v208
	ds_read_b128 v[140:143], v160
	v_add_u32_e32 v160, 0x20d10, v208
	ds_read_b128 v[144:147], v160
	v_add_u32_e32 v160, 0x20f10, v208
	ds_read_b128 v[148:151], v160
	s_waitcnt lgkmcnt(0)
; #define GAS __attribute__((address_space(1)))
; #define PG8_LAS __attribute__((address_space(3)))
;     __device__ __forceinline__ void operator()(const i32x4 (&acc)[2][2][4][2], const Unit& u, int wr, int wc, int fr, int fq, PG8_LAS unsigned* scr) const {
;     ...
;         for (int n = 0; n < 2; ++n) { bgv[n] = *(const PG8_LAS f32x4*)(scr + 512 + cl + 4 * n) * C2; buv[n] = *(const PG8_LAS f32x4*)(scr + 512 + 128 + cl + 4 * n);
;             csg[n] = *(const PG8_LAS f32x4*)(scr + 256 + cl + 4 * n) * (C2 / 127.0f); csu[n] = *(const PG8_LAS f32x4*)(scr + 256 + 128 + cl + 4 * n) * (1.0f / 127.0f); }
; #pragma unroll
;         for (int ai = 0; ai < 2; ++ai)
; #pragma unroll
;             for (int mp = 0; mp < 4; mp += 2) { unsigned wp[2][2];
; #pragma unroll
;                 for (int hm = 0; hm < 2; ++hm) { const int m = mp + hm; const int r = ai * HALF + wr * 64 + m * 16 + fr; const float rs = __uint_as_float(scr[r]); float o[8];
; #pragma unroll
;                     for (int n = 0; n < 2; ++n) { const f32x4 sgr = csg[n] * rs, sur = csu[n] * rs;
; #pragma unroll
;                         for (int q = 0; q < 4; ++q) { const float h = fminf(__builtin_fmaf((float)acc[ai][0][m][n][q], sgr[q], bgv[n][q]), 7.0f * C2), up = fminf(fmaxf(__builtin_fmaf((float)acc[ai][1][m][n][q], sur[q], buv[n][q]), -7.0f), 7.0f);
;                             const float sg = __builtin_amdgcn_rcpf(1.0f + __builtin_amdgcn_exp2f(-h)); o[4 * n + q] = __builtin_fmaf(up, ACT_SC / C2, ACT_SC / C2) * (h * sg); } }
;                     int w0 = __builtin_amdgcn_cvt_pk_fp8_f32(o[0], o[1], 0, false); w0 = __builtin_amdgcn_cvt_pk_fp8_f32(o[2], o[3], w0, true);
;                     int w1 = __builtin_amdgcn_cvt_pk_fp8_f32(o[4], o[5], 0, false); w1 = __builtin_amdgcn_cvt_pk_fp8_f32(o[6], o[7], w1, true);
;                     wp[hm][0] = (unsigned)w0; wp[hm][1] = (unsigned)w1; }
;                 { auto r0 = __builtin_amdgcn_permlane16_swap(wp[0][0], wp[1][0], false, false); wp[0][0] = r0[0]; wp[1][0] = r0[1];
;                   auto r1 = __builtin_amdgcn_permlane16_swap(wp[0][1], wp[1][1], false, false); wp[0][1] = r1[0]; wp[1][1] = r1[1]; }
;                 const int odd = fq & 1;
;                 const size_t arow = (size_t)(row0 + ai * HALF + (mp + odd) * 16);
;                 *(GAS u32x4*)(act + arow * 1024 + (c0 - 8 * odd)) = (u32x4){wp[0][0], wp[0][1], wp[1][0], wp[1][1]};
	v_mul_f32_e32 v136, 0x401d265f, v136
	v_mul_f32_e32 v137, 0x401d265f, v137
	v_mul_f32_e32 v138, 0x401d265f, v138
	v_mul_f32_e32 v139, 0x401d265f, v139
	v_mul_f32_e32 v144, 0x3c9e6325, v144
	v_mul_f32_e32 v145, 0x3c9e6325, v145
	v_mul_f32_e32 v146, 0x3c9e6325, v146
	v_mul_f32_e32 v147, 0x3c9e6325, v147
	v_mul_f32_e32 v148, 0x3c010204, v148
	v_mul_f32_e32 v149, 0x3c010204, v149
	v_mul_f32_e32 v150, 0x3c010204, v150
	v_mul_f32_e32 v151, 0x3c010204, v151
	v_cvt_f32_i32_e32 v120, v120
	v_cvt_f32_i32_e32 v121, v121
	v_cvt_f32_i32_e32 v122, v122
	v_cvt_f32_i32_e32 v123, v123
	v_cvt_f32_i32_e32 v124, v124
	v_cvt_f32_i32_e32 v125, v125
	v_cvt_f32_i32_e32 v126, v126
	v_cvt_f32_i32_e32 v127, v127
	v_pk_mul_f32 v[160:161], v[144:145], v[152:153] op_sel_hi:[1,0]
	v_pk_mul_f32 v[162:163], v[146:147], v[152:153] op_sel_hi:[1,0]
	v_pk_fma_f32 v[120:121], v[120:121], v[160:161], v[136:137]
	v_pk_fma_f32 v[122:123], v[122:123], v[162:163], v[138:139]
	v_pk_mul_f32 v[160:161], v[148:149], v[152:153] op_sel_hi:[1,0]
	v_pk_mul_f32 v[162:163], v[150:151], v[152:153] op_sel_hi:[1,0]
	v_min_f32_e32 v120, 0x41898193, v120
	v_min_f32_e32 v121, 0x41898193, v121
	v_min_f32_e32 v122, 0x41898193, v122
	v_min_f32_e32 v123, 0x41898193, v123
	v_pk_fma_f32 v[124:125], v[124:125], v[160:161], v[140:141]
	v_pk_fma_f32 v[126:127], v[126:127], v[162:163], v[142:143]
	v_exp_f32_e64 v160, -v120
	v_exp_f32_e64 v161, -v121
	v_exp_f32_e64 v162, -v122
	v_exp_f32_e64 v163, -v123
	v_med3_f32 v124, v124, s8, v199
	v_med3_f32 v125, v125, s8, v199
	v_med3_f32 v126, v126, s8, v199
	v_med3_f32 v127, v127, s8, v199
	v_pk_add_f32 v[160:161], v[160:161], 1.0 op_sel_hi:[1,0]
	v_pk_add_f32 v[162:163], v[162:163], 1.0 op_sel_hi:[1,0]
	v_pk_fma_f32 v[124:125], v[124:125], s[100:101], s[100:101]
	v_pk_fma_f32 v[126:127], v[126:127], s[100:101], s[100:101]
	v_rcp_f32_e32 v160, v160
	v_rcp_f32_e32 v161, v161
	v_rcp_f32_e32 v162, v162
	v_rcp_f32_e32 v163, v163
	v_nop
	v_pk_mul_f32 v[120:121], v[120:121], v[160:161]
	v_pk_mul_f32 v[122:123], v[122:123], v[162:163]
	v_pk_mul_f32 v[120:121], v[124:125], v[120:121]
	v_pk_mul_f32 v[122:123], v[126:127], v[122:123]
	v_cvt_pk_fp8_f32 v129, v120, v121
	v_cvt_pk_fp8_f32 v129, v122, v123 op_sel:[0,0,1]
	v_cvt_f32_i32_e32 v104, v104
	v_cvt_f32_i32_e32 v105, v105
	v_cvt_f32_i32_e32 v106, v106
	v_cvt_f32_i32_e32 v107, v107
	v_cvt_f32_i32_e32 v108, v108
	v_cvt_f32_i32_e32 v109, v109
	v_cvt_f32_i32_e32 v110, v110
	v_cvt_f32_i32_e32 v111, v111
	v_pk_mul_f32 v[202:203], v[144:145], v[152:153] op_sel:[0,1] op_sel_hi:[1,1]
	v_pk_mul_f32 v[204:205], v[146:147], v[152:153] op_sel:[0,1] op_sel_hi:[1,1]
	v_pk_fma_f32 v[104:105], v[104:105], v[202:203], v[136:137]
	v_pk_fma_f32 v[106:107], v[106:107], v[204:205], v[138:139]
	v_pk_mul_f32 v[202:203], v[148:149], v[152:153] op_sel:[0,1] op_sel_hi:[1,1]
	v_pk_mul_f32 v[204:205], v[150:151], v[152:153] op_sel:[0,1] op_sel_hi:[1,1]
	v_min_f32_e32 v104, 0x41898193, v104
	v_min_f32_e32 v105, 0x41898193, v105
	v_min_f32_e32 v106, 0x41898193, v106
	v_min_f32_e32 v107, 0x41898193, v107
	v_pk_fma_f32 v[108:109], v[108:109], v[202:203], v[140:141]
	v_pk_fma_f32 v[110:111], v[110:111], v[204:205], v[142:143]
	v_exp_f32_e64 v202, -v104
	v_exp_f32_e64 v203, -v105
	v_exp_f32_e64 v204, -v106
	v_exp_f32_e64 v205, -v107
	v_med3_f32 v108, v108, s8, v199
	v_med3_f32 v109, v109, s8, v199
	v_med3_f32 v110, v110, s8, v199
	v_med3_f32 v111, v111, s8, v199
	v_pk_add_f32 v[202:203], v[202:203], 1.0 op_sel_hi:[1,0]
	v_pk_add_f32 v[204:205], v[204:205], 1.0 op_sel_hi:[1,0]
	v_pk_fma_f32 v[108:109], v[108:109], s[100:101], s[100:101]
	v_pk_fma_f32 v[110:111], v[110:111], s[100:101], s[100:101]
	v_rcp_f32_e32 v202, v202
	v_rcp_f32_e32 v203, v203
	v_rcp_f32_e32 v204, v204
	v_rcp_f32_e32 v205, v205
	v_nop
	v_pk_mul_f32 v[104:105], v[104:105], v[202:203]
	v_pk_mul_f32 v[106:107], v[106:107], v[204:205]
	v_pk_mul_f32 v[104:105], v[108:109], v[104:105]
	v_pk_mul_f32 v[106:107], v[110:111], v[106:107]
	v_cvt_pk_fp8_f32 v131, v104, v105
	v_cvt_pk_fp8_f32 v131, v106, v107 op_sel:[0,0,1]
	s_nop 1
	v_permlane16_swap_b32_e32 v128, v130
	v_permlane16_swap_b32_e32 v129, v131
	v_add_u32_e32 v160, 0, v185
	v_mov_b32_e32 v161, 0
	v_lshlrev_b64 v[160:161], 10, v[160:161]
	v_lshl_add_u64 v[160:161], s[60:61], 0, v[160:161]
	v_lshl_add_u64 v[160:161], v[160:161], 0, v[206:207]
	global_store_dwordx4 v[160:161], v[128:131], off
	v_cvt_f32_i32_e32 v88, v88
	v_cvt_f32_i32_e32 v89, v89
	v_cvt_f32_i32_e32 v90, v90
	v_cvt_f32_i32_e32 v91, v91
	v_cvt_f32_i32_e32 v92, v92
	v_cvt_f32_i32_e32 v93, v93
	v_cvt_f32_i32_e32 v94, v94
	v_cvt_f32_i32_e32 v95, v95
	v_pk_mul_f32 v[160:161], v[144:145], v[154:155] op_sel_hi:[1,0]
	v_pk_mul_f32 v[162:163], v[146:147], v[154:155] op_sel_hi:[1,0]
	v_pk_fma_f32 v[88:89], v[88:89], v[160:161], v[136:137]
	v_pk_fma_f32 v[90:91], v[90:91], v[162:163], v[138:139]
	v_pk_mul_f32 v[160:161], v[148:149], v[154:155] op_sel_hi:[1,0]
	v_pk_mul_f32 v[162:163], v[150:151], v[154:155] op_sel_hi:[1,0]
	v_min_f32_e32 v88, 0x41898193, v88
	v_min_f32_e32 v89, 0x41898193, v89
	v_min_f32_e32 v90, 0x41898193, v90
	v_min_f32_e32 v91, 0x41898193, v91
	v_pk_fma_f32 v[92:93], v[92:93], v[160:161], v[140:141]
	v_pk_fma_f32 v[94:95], v[94:95], v[162:163], v[142:143]
	v_exp_f32_e64 v160, -v88
	v_exp_f32_e64 v161, -v89
	v_exp_f32_e64 v162, -v90
	v_exp_f32_e64 v163, -v91
	v_med3_f32 v92, v92, s8, v199
	v_med3_f32 v93, v93, s8, v199
	v_med3_f32 v94, v94, s8, v199
	v_med3_f32 v95, v95, s8, v199
	v_pk_add_f32 v[160:161], v[160:161], 1.0 op_sel_hi:[1,0]
	v_pk_add_f32 v[162:163], v[162:163], 1.0 op_sel_hi:[1,0]
	v_pk_fma_f32 v[92:93], v[92:93], s[100:101], s[100:101]
; #define GAS __attribute__((address_space(1)))
;     __device__ __forceinline__ void operator()(const i32x4 (&acc)[2][2][4][2], const Unit& u, int wr, int wc, int fr, int fq, PG8_LAS unsigned* scr) const {
;     ...
;                 for (int hm = 0; hm < 2; ++hm) { const int m = mp + hm; const int r = ai * HALF + wr * 64 + m * 16 + fr; const float rs = __uint_as_float(scr[r]); float o[8];
; #pragma unroll
;                     for (int n = 0; n < 2; ++n) { const f32x4 sgr = csg[n] * rs, sur = csu[n] * rs;
; #pragma unroll
;                         for (int q = 0; q < 4; ++q) { const float h = fminf(__builtin_fmaf((float)acc[ai][0][m][n][q], sgr[q], bgv[n][q]), 7.0f * C2), up = fminf(fmaxf(__builtin_fmaf((float)acc[ai][1][m][n][q], sur[q], buv[n][q]), -7.0f), 7.0f);
;                             const float sg = __builtin_amdgcn_rcpf(1.0f + __builtin_amdgcn_exp2f(-h)); o[4 * n + q] = __builtin_fmaf(up, ACT_SC / C2, ACT_SC / C2) * (h * sg); } }
;                     int w0 = __builtin_amdgcn_cvt_pk_fp8_f32(o[0], o[1], 0, false); w0 = __builtin_amdgcn_cvt_pk_fp8_f32(o[2], o[3], w0, true);
;                     int w1 = __builtin_amdgcn_cvt_pk_fp8_f32(o[4], o[5], 0, false); w1 = __builtin_amdgcn_cvt_pk_fp8_f32(o[6], o[7], w1, true);
;                     wp[hm][0] = (unsigned)w0; wp[hm][1] = (unsigned)w1; }
;                 { auto r0 = __builtin_amdgcn_permlane16_swap(wp[0][0], wp[1][0], false, false); wp[0][0] = r0[0]; wp[1][0] = r0[1];
;                   auto r1 = __builtin_amdgcn_permlane16_swap(wp[0][1], wp[1][1], false, false); wp[0][1] = r1[0]; wp[1][1] = r1[1]; }
;                 const int odd = fq & 1;
;                 const size_t arow = (size_t)(row0 + ai * HALF + (mp + odd) * 16);
;                 *(GAS u32x4*)(act + arow * 1024 + (c0 - 8 * odd)) = (u32x4){wp[0][0], wp[0][1], wp[1][0], wp[1][1]};
	v_pk_fma_f32 v[94:95], v[94:95], s[100:101], s[100:101]
	v_rcp_f32_e32 v160, v160
	v_rcp_f32_e32 v161, v161
	v_rcp_f32_e32 v162, v162
	v_rcp_f32_e32 v163, v163
	v_nop
	v_pk_mul_f32 v[88:89], v[88:89], v[160:161]
	v_pk_mul_f32 v[90:91], v[90:91], v[162:163]
	v_pk_mul_f32 v[88:89], v[92:93], v[88:89]
	v_pk_mul_f32 v[90:91], v[94:95], v[90:91]
	v_cvt_pk_fp8_f32 v97, v88, v89
	v_cvt_pk_fp8_f32 v97, v90, v91 op_sel:[0,0,1]
	v_cvt_f32_i32_e32 v72, v72
	v_cvt_f32_i32_e32 v73, v73
	v_cvt_f32_i32_e32 v74, v74
	v_cvt_f32_i32_e32 v75, v75
	v_cvt_f32_i32_e32 v76, v76
	v_cvt_f32_i32_e32 v77, v77
	v_cvt_f32_i32_e32 v78, v78
	v_cvt_f32_i32_e32 v79, v79
	v_pk_mul_f32 v[202:203], v[144:145], v[154:155] op_sel:[0,1] op_sel_hi:[1,1]
	v_pk_mul_f32 v[204:205], v[146:147], v[154:155] op_sel:[0,1] op_sel_hi:[1,1]
	v_pk_fma_f32 v[72:73], v[72:73], v[202:203], v[136:137]
	v_pk_fma_f32 v[74:75], v[74:75], v[204:205], v[138:139]
	v_pk_mul_f32 v[202:203], v[148:149], v[154:155] op_sel:[0,1] op_sel_hi:[1,1]
	v_pk_mul_f32 v[204:205], v[150:151], v[154:155] op_sel:[0,1] op_sel_hi:[1,1]
	v_min_f32_e32 v72, 0x41898193, v72
	v_min_f32_e32 v73, 0x41898193, v73
	v_min_f32_e32 v74, 0x41898193, v74
	v_min_f32_e32 v75, 0x41898193, v75
	v_pk_fma_f32 v[76:77], v[76:77], v[202:203], v[140:141]
	v_pk_fma_f32 v[78:79], v[78:79], v[204:205], v[142:143]
	v_exp_f32_e64 v202, -v72
	v_exp_f32_e64 v203, -v73
	v_exp_f32_e64 v204, -v74
	v_exp_f32_e64 v205, -v75
	v_med3_f32 v76, v76, s8, v199
	v_med3_f32 v77, v77, s8, v199
	v_med3_f32 v78, v78, s8, v199
	v_med3_f32 v79, v79, s8, v199
	v_pk_add_f32 v[202:203], v[202:203], 1.0 op_sel_hi:[1,0]
	v_pk_add_f32 v[204:205], v[204:205], 1.0 op_sel_hi:[1,0]
	v_pk_fma_f32 v[76:77], v[76:77], s[100:101], s[100:101]
	v_pk_fma_f32 v[78:79], v[78:79], s[100:101], s[100:101]
	v_rcp_f32_e32 v202, v202
	v_rcp_f32_e32 v203, v203
	v_rcp_f32_e32 v204, v204
	v_rcp_f32_e32 v205, v205
	v_nop
	v_pk_mul_f32 v[72:73], v[72:73], v[202:203]
	v_pk_mul_f32 v[74:75], v[74:75], v[204:205]
	v_pk_mul_f32 v[72:73], v[76:77], v[72:73]
	v_pk_mul_f32 v[74:75], v[78:79], v[74:75]
	v_cvt_pk_fp8_f32 v99, v72, v73
	v_cvt_pk_fp8_f32 v99, v74, v75 op_sel:[0,0,1]
	s_nop 1
	v_permlane16_swap_b32_e32 v96, v98
	v_permlane16_swap_b32_e32 v97, v99
	v_add_u32_e32 v160, 32, v185
	v_mov_b32_e32 v161, 0
	v_lshlrev_b64 v[160:161], 10, v[160:161]
	v_lshl_add_u64 v[160:161], s[60:61], 0, v[160:161]
	v_lshl_add_u64 v[160:161], v[160:161], 0, v[206:207]
	global_store_dwordx4 v[160:161], v[96:99], off
	v_cvt_f32_i32_e32 v56, v56
	v_cvt_f32_i32_e32 v57, v57
	v_cvt_f32_i32_e32 v58, v58
	v_cvt_f32_i32_e32 v59, v59
	v_cvt_f32_i32_e32 v60, v60
	v_cvt_f32_i32_e32 v61, v61
	v_cvt_f32_i32_e32 v62, v62
	v_cvt_f32_i32_e32 v63, v63
	v_pk_mul_f32 v[160:161], v[144:145], v[156:157] op_sel_hi:[1,0]
	v_pk_mul_f32 v[162:163], v[146:147], v[156:157] op_sel_hi:[1,0]
	v_pk_fma_f32 v[56:57], v[56:57], v[160:161], v[136:137]
	v_pk_fma_f32 v[58:59], v[58:59], v[162:163], v[138:139]
	v_pk_mul_f32 v[160:161], v[148:149], v[156:157] op_sel_hi:[1,0]
	v_pk_mul_f32 v[162:163], v[150:151], v[156:157] op_sel_hi:[1,0]
	v_min_f32_e32 v56, 0x41898193, v56
	v_min_f32_e32 v57, 0x41898193, v57
	v_min_f32_e32 v58, 0x41898193, v58
	v_min_f32_e32 v59, 0x41898193, v59
	v_pk_fma_f32 v[60:61], v[60:61], v[160:161], v[140:141]
	v_pk_fma_f32 v[62:63], v[62:63], v[162:163], v[142:143]
	v_exp_f32_e64 v160, -v56
	v_exp_f32_e64 v161, -v57
	v_exp_f32_e64 v162, -v58
	v_exp_f32_e64 v163, -v59
	v_med3_f32 v60, v60, s8, v199
	v_med3_f32 v61, v61, s8, v199
	v_med3_f32 v62, v62, s8, v199
	v_med3_f32 v63, v63, s8, v199
	v_pk_add_f32 v[160:161], v[160:161], 1.0 op_sel_hi:[1,0]
	v_pk_add_f32 v[162:163], v[162:163], 1.0 op_sel_hi:[1,0]
	v_pk_fma_f32 v[60:61], v[60:61], s[100:101], s[100:101]
	v_pk_fma_f32 v[62:63], v[62:63], s[100:101], s[100:101]
	v_rcp_f32_e32 v160, v160
	v_rcp_f32_e32 v161, v161
	v_rcp_f32_e32 v162, v162
	v_rcp_f32_e32 v163, v163
	v_nop
	v_pk_mul_f32 v[56:57], v[56:57], v[160:161]
	v_pk_mul_f32 v[58:59], v[58:59], v[162:163]
	v_pk_mul_f32 v[56:57], v[60:61], v[56:57]
	v_pk_mul_f32 v[58:59], v[62:63], v[58:59]
	v_cvt_pk_fp8_f32 v65, v56, v57
	v_cvt_pk_fp8_f32 v65, v58, v59 op_sel:[0,0,1]
	v_cvt_f32_i32_e32 v32, v32
	v_cvt_f32_i32_e32 v33, v33
	v_cvt_f32_i32_e32 v34, v34
	v_cvt_f32_i32_e32 v35, v35
	v_cvt_f32_i32_e32 v36, v36
	v_cvt_f32_i32_e32 v37, v37
	v_cvt_f32_i32_e32 v38, v38
	v_cvt_f32_i32_e32 v39, v39
	v_pk_mul_f32 v[202:203], v[144:145], v[156:157] op_sel:[0,1] op_sel_hi:[1,1]
	v_pk_mul_f32 v[204:205], v[146:147], v[156:157] op_sel:[0,1] op_sel_hi:[1,1]
	v_pk_fma_f32 v[32:33], v[32:33], v[202:203], v[136:137]
	v_pk_fma_f32 v[34:35], v[34:35], v[204:205], v[138:139]
	v_pk_mul_f32 v[202:203], v[148:149], v[156:157] op_sel:[0,1] op_sel_hi:[1,1]
	v_pk_mul_f32 v[204:205], v[150:151], v[156:157] op_sel:[0,1] op_sel_hi:[1,1]
	v_min_f32_e32 v32, 0x41898193, v32
	v_min_f32_e32 v33, 0x41898193, v33
	v_min_f32_e32 v34, 0x41898193, v34
	v_min_f32_e32 v35, 0x41898193, v35
	v_pk_fma_f32 v[36:37], v[36:37], v[202:203], v[140:141]
; #define GAS __attribute__((address_space(1)))
; #define PG8_BAR __builtin_amdgcn_s_barrier()
;     __device__ __forceinline__ void operator()(const i32x4 (&acc)[2][2][4][2], const Unit& u, int wr, int wc, int fr, int fq, PG8_LAS unsigned* scr) const {
;     ...
;                 for (int hm = 0; hm < 2; ++hm) { const int m = mp + hm; const int r = ai * HALF + wr * 64 + m * 16 + fr; const float rs = __uint_as_float(scr[r]); float o[8];
; #pragma unroll
;                     for (int n = 0; n < 2; ++n) { const f32x4 sgr = csg[n] * rs, sur = csu[n] * rs;
; #pragma unroll
;                         for (int q = 0; q < 4; ++q) { const float h = fminf(__builtin_fmaf((float)acc[ai][0][m][n][q], sgr[q], bgv[n][q]), 7.0f * C2), up = fminf(fmaxf(__builtin_fmaf((float)acc[ai][1][m][n][q], sur[q], buv[n][q]), -7.0f), 7.0f);
;                             const float sg = __builtin_amdgcn_rcpf(1.0f + __builtin_amdgcn_exp2f(-h)); o[4 * n + q] = __builtin_fmaf(up, ACT_SC / C2, ACT_SC / C2) * (h * sg); } }
;                     int w0 = __builtin_amdgcn_cvt_pk_fp8_f32(o[0], o[1], 0, false); w0 = __builtin_amdgcn_cvt_pk_fp8_f32(o[2], o[3], w0, true);
;                     int w1 = __builtin_amdgcn_cvt_pk_fp8_f32(o[4], o[5], 0, false); w1 = __builtin_amdgcn_cvt_pk_fp8_f32(o[6], o[7], w1, true);
;                     wp[hm][0] = (unsigned)w0; wp[hm][1] = (unsigned)w1; }
;                 { auto r0 = __builtin_amdgcn_permlane16_swap(wp[0][0], wp[1][0], false, false); wp[0][0] = r0[0]; wp[1][0] = r0[1];
;                   auto r1 = __builtin_amdgcn_permlane16_swap(wp[0][1], wp[1][1], false, false); wp[0][1] = r1[0]; wp[1][1] = r1[1]; }
;                 const int odd = fq & 1;
;                 const size_t arow = (size_t)(row0 + ai * HALF + (mp + odd) * 16);
;                 *(GAS u32x4*)(act + arow * 1024 + (c0 - 8 * odd)) = (u32x4){wp[0][0], wp[0][1], wp[1][0], wp[1][1]};
; template <class Epi, class Sched, bool GATHER, int MODE>
; __device__ __forceinline__ void gemm_phase(PG8_LAS unsigned char* lds, PG8_LAS unsigned* scr, const Gemm g, const Sched& S, const Epi& E, int tid_in) {
;     ...
;         if (!has_next) break;
;         cur = nxt; cA = nA; cB = nB; ++ui;
;         if (GATHER) { const u32x4 nx = gather_read(cur); c0[0] = nx[0]; c0[1] = nx[1]; c1[0] = nx[2]; c1[1] = nx[3]; }
;         if (wr == 1) PG8_BAR;
	v_pk_fma_f32 v[38:39], v[38:39], v[204:205], v[142:143]
	v_exp_f32_e64 v202, -v32
	v_exp_f32_e64 v203, -v33
	v_exp_f32_e64 v204, -v34
	v_exp_f32_e64 v205, -v35
	v_med3_f32 v36, v36, s8, v199
	v_med3_f32 v37, v37, s8, v199
	v_med3_f32 v38, v38, s8, v199
	v_med3_f32 v39, v39, s8, v199
	v_pk_add_f32 v[202:203], v[202:203], 1.0 op_sel_hi:[1,0]
	v_pk_add_f32 v[204:205], v[204:205], 1.0 op_sel_hi:[1,0]
	v_pk_fma_f32 v[36:37], v[36:37], s[100:101], s[100:101]
	v_pk_fma_f32 v[38:39], v[38:39], s[100:101], s[100:101]
	v_rcp_f32_e32 v202, v202
	v_rcp_f32_e32 v203, v203
	v_rcp_f32_e32 v204, v204
	v_rcp_f32_e32 v205, v205
	v_nop
	v_pk_mul_f32 v[32:33], v[32:33], v[202:203]
	v_pk_mul_f32 v[34:35], v[34:35], v[204:205]
	v_pk_mul_f32 v[32:33], v[36:37], v[32:33]
	v_pk_mul_f32 v[34:35], v[38:39], v[34:35]
	v_cvt_pk_fp8_f32 v67, v32, v33
	v_cvt_pk_fp8_f32 v67, v34, v35 op_sel:[0,0,1]
	s_nop 1
	v_permlane16_swap_b32_e32 v64, v66
	v_permlane16_swap_b32_e32 v65, v67
	v_add_u32_e32 v160, 128, v185
	v_mov_b32_e32 v161, 0
	v_lshlrev_b64 v[160:161], 10, v[160:161]
	v_lshl_add_u64 v[160:161], s[60:61], 0, v[160:161]
	v_lshl_add_u64 v[160:161], v[160:161], 0, v[206:207]
	global_store_dwordx4 v[160:161], v[64:67], off
	v_cvt_f32_i32_e32 v16, v16
	v_cvt_f32_i32_e32 v17, v17
	v_cvt_f32_i32_e32 v18, v18
	v_cvt_f32_i32_e32 v19, v19
	v_cvt_f32_i32_e32 v20, v20
	v_cvt_f32_i32_e32 v21, v21
	v_cvt_f32_i32_e32 v22, v22
	v_cvt_f32_i32_e32 v23, v23
	v_pk_mul_f32 v[160:161], v[144:145], v[158:159] op_sel_hi:[1,0]
	v_pk_mul_f32 v[162:163], v[146:147], v[158:159] op_sel_hi:[1,0]
	v_pk_fma_f32 v[16:17], v[16:17], v[160:161], v[136:137]
	v_pk_fma_f32 v[18:19], v[18:19], v[162:163], v[138:139]
	v_pk_mul_f32 v[160:161], v[148:149], v[158:159] op_sel_hi:[1,0]
	v_pk_mul_f32 v[162:163], v[150:151], v[158:159] op_sel_hi:[1,0]
	v_min_f32_e32 v16, 0x41898193, v16
	v_min_f32_e32 v17, 0x41898193, v17
	v_min_f32_e32 v18, 0x41898193, v18
	v_min_f32_e32 v19, 0x41898193, v19
	v_pk_fma_f32 v[20:21], v[20:21], v[160:161], v[140:141]
	v_pk_fma_f32 v[22:23], v[22:23], v[162:163], v[142:143]
	v_exp_f32_e64 v160, -v16
	v_exp_f32_e64 v161, -v17
	v_exp_f32_e64 v162, -v18
	v_exp_f32_e64 v163, -v19
	v_med3_f32 v20, v20, s8, v199
	v_med3_f32 v21, v21, s8, v199
	v_med3_f32 v22, v22, s8, v199
	v_med3_f32 v23, v23, s8, v199
	v_pk_add_f32 v[160:161], v[160:161], 1.0 op_sel_hi:[1,0]
	v_pk_add_f32 v[162:163], v[162:163], 1.0 op_sel_hi:[1,0]
	v_pk_fma_f32 v[20:21], v[20:21], s[100:101], s[100:101]
	v_pk_fma_f32 v[22:23], v[22:23], s[100:101], s[100:101]
	v_rcp_f32_e32 v160, v160
	v_rcp_f32_e32 v161, v161
	v_rcp_f32_e32 v162, v162
	v_rcp_f32_e32 v163, v163
	v_nop
	v_pk_mul_f32 v[16:17], v[16:17], v[160:161]
	v_pk_mul_f32 v[18:19], v[18:19], v[162:163]
	v_pk_mul_f32 v[16:17], v[20:21], v[16:17]
	v_pk_mul_f32 v[18:19], v[22:23], v[18:19]
	v_cvt_pk_fp8_f32 v25, v16, v17
	v_cvt_pk_fp8_f32 v25, v18, v19 op_sel:[0,0,1]
	v_cvt_f32_i32_e32 v0, v0
	v_cvt_f32_i32_e32 v1, v1
	v_cvt_f32_i32_e32 v2, v2
	v_cvt_f32_i32_e32 v3, v3
	v_cvt_f32_i32_e32 v4, v4
	v_cvt_f32_i32_e32 v5, v5
	v_cvt_f32_i32_e32 v6, v6
	v_cvt_f32_i32_e32 v7, v7
	v_pk_mul_f32 v[202:203], v[144:145], v[158:159] op_sel:[0,1] op_sel_hi:[1,1]
	v_pk_mul_f32 v[204:205], v[146:147], v[158:159] op_sel:[0,1] op_sel_hi:[1,1]
	v_pk_fma_f32 v[0:1], v[0:1], v[202:203], v[136:137]
	v_pk_fma_f32 v[2:3], v[2:3], v[204:205], v[138:139]
	v_pk_mul_f32 v[202:203], v[148:149], v[158:159] op_sel:[0,1] op_sel_hi:[1,1]
	v_pk_mul_f32 v[204:205], v[150:151], v[158:159] op_sel:[0,1] op_sel_hi:[1,1]
	v_min_f32_e32 v0, 0x41898193, v0
	v_min_f32_e32 v1, 0x41898193, v1
	v_min_f32_e32 v2, 0x41898193, v2
	v_min_f32_e32 v3, 0x41898193, v3
	v_pk_fma_f32 v[4:5], v[4:5], v[202:203], v[140:141]
	v_pk_fma_f32 v[6:7], v[6:7], v[204:205], v[142:143]
	v_exp_f32_e64 v202, -v0
	v_exp_f32_e64 v203, -v1
	v_exp_f32_e64 v204, -v2
	v_exp_f32_e64 v205, -v3
	v_med3_f32 v4, v4, s8, v199
	v_med3_f32 v5, v5, s8, v199
	v_med3_f32 v6, v6, s8, v199
	v_med3_f32 v7, v7, s8, v199
	v_pk_add_f32 v[202:203], v[202:203], 1.0 op_sel_hi:[1,0]
	v_pk_add_f32 v[204:205], v[204:205], 1.0 op_sel_hi:[1,0]
	v_pk_fma_f32 v[4:5], v[4:5], s[100:101], s[100:101]
	v_pk_fma_f32 v[6:7], v[6:7], s[100:101], s[100:101]
	v_rcp_f32_e32 v202, v202
	v_rcp_f32_e32 v203, v203
	v_rcp_f32_e32 v204, v204
	v_rcp_f32_e32 v205, v205
	v_nop
	v_pk_mul_f32 v[0:1], v[0:1], v[202:203]
	v_pk_mul_f32 v[2:3], v[2:3], v[204:205]
	v_pk_mul_f32 v[0:1], v[4:5], v[0:1]
	v_pk_mul_f32 v[2:3], v[6:7], v[2:3]
	v_cvt_pk_fp8_f32 v27, v0, v1
	v_cvt_pk_fp8_f32 v27, v2, v3 op_sel:[0,0,1]
	s_nop 1
	v_permlane16_swap_b32_e32 v24, v26
	v_permlane16_swap_b32_e32 v25, v27
	v_add_u32_e32 v160, 160, v185
	v_mov_b32_e32 v161, 0
	v_lshlrev_b64 v[160:161], 10, v[160:161]
	v_lshl_add_u64 v[160:161], s[60:61], 0, v[160:161]
	v_lshl_add_u64 v[160:161], v[160:161], 0, v[206:207]
	global_store_dwordx4 v[160:161], v[24:27], off
	s_cmp_eq_u32 s38, s89
	s_mov_b64 s[10:11], -1
	s_cbranch_scc1 .LBB0_786
	s_andn2_b64 vcc, exec, s[58:59]
	s_cbranch_vccnz .LBB0_785
	s_barrier
	s_branch .LBB0_785
